# v76 + phase H idle-time weight conversion claims 64 items per idle workgroup instead of 144 (rest converted in phase A of layer 1)
# baseline (speedup 1.0000x reference)
.LBB0_4033:
	v_readlane_b32 s2, v254, 0
	v_readlane_b32 s3, v254, 1
	s_load_dword s0, s[2:3], 0x128
	v_readlane_b32 s4, v254, 50
	s_add_i32 s24, s4, 8
	s_waitcnt lgkmcnt(0)
	s_cmp_le_i32 s0, s24
	s_cbranch_scc0 .LBB0_4887
	s_load_dword s0, s[2:3], 0x12c
	s_waitcnt lgkmcnt(0)
	s_cmp_ge_i32 s24, s0
	s_cbranch_scc1 .LBB0_4887
	v_readlane_b32 s10, v254, 0
	v_readlane_b32 s11, v254, 1
	s_load_dwordx2 s[8:9], s[10:11], 0x120
	s_mov_b32 s25, s43
	s_cmpk_gt_i32 s25, 0x9f
	v_readlane_b32 s4, v254, 31
	s_cselect_b64 s[2:3], -1, 0
	v_readlane_b32 s5, v254, 32
	s_and_b64 s[2:3], s[4:5], s[2:3]
	s_waitcnt vmcnt(0)
	v_mov_b32_e32 v161, v235
	v_readlane_b32 s26, v254, 6
	s_andn2_b64 vcc, exec, s[2:3]
	s_cbranch_vccnz .LBB0_4850
	v_cmp_eq_u32_e32 vcc, 0, v161
	s_and_saveexec_b64 s[2:3], vcc
	s_cbranch_execz .LBB0_4040
	s_mov_b64 s[6:7], exec
	v_mbcnt_lo_u32_b32 v0, s6, 0
	v_mbcnt_hi_u32_b32 v0, s7, v0
	v_cmp_eq_u32_e32 vcc, 0, v0
	s_and_saveexec_b64 s[4:5], vcc
	s_cbranch_execz .LBB0_4039
	s_bcnt1_i32_b64 s0, s[6:7]
	s_mulk_i32 s0, 0x40
	v_mov_b32_e32 v2, s0
	v_mov_b32_e32 v3, 0x38000
	s_waitcnt lgkmcnt(0)
	global_atomic_add v2, v3, v2, s[8:9] sc0
.LBB0_4039:
	s_or_b64 exec, exec, s[4:5]
	s_waitcnt vmcnt(0)
	v_readfirstlane_b32 s0, v2
	s_nop 1
	v_mov_b32_e32 v2, s0
	s_movk_i32 s0, 0x40
	v_mad_u32_u24 v0, v0, s0, v2
	v_readlane_b32 s0, v254, 28
	s_nop 1
	v_mov_b32_e32 v2, s0
	ds_write_b32 v2, v0
.LBB0_4040:
	s_or_b64 exec, exec, s[2:3]
	v_readlane_b32 s0, v254, 28
	s_waitcnt lgkmcnt(0)
	s_barrier
	v_mov_b32_e32 v0, s0
	ds_read_b32 v0, v0
	s_waitcnt lgkmcnt(0)
	s_barrier
	v_readfirstlane_b32 s27, v0
	s_cmp_gt_i32 s27, 0xbfff
	s_cbranch_scc1 .LBB0_4850
	s_min_i32 s16, s27, 0xbfc0
	s_addk_i32 s16, 0x40
	s_add_i32 s27, s27, s26
	s_cmp_ge_i32 s27, s16
	s_cbranch_scc1 .LBB0_4850
	s_mul_hi_i32 s0, s27, 0x2aaaaaab
	s_lshr_b32 s2, s0, 31
	s_ashr_i32 s0, s0, 9
	s_add_i32 s2, s0, s2
	s_mul_i32 s0, s2, 0xc00
	s_sub_i32 s0, s27, s0
	s_cmpk_gt_i32 s0, 0x7ff
	s_mov_b64 s[6:7], -1
	s_cbranch_scc0 .LBB0_4044
	s_load_dwordx2 s[4:5], s[10:11], 0x108
	s_and_b32 s6, s0, 0x7fffffc0
	s_ashr_i32 s3, s2, 31
	s_add_i32 s92, s6, 0xfffff800
	s_lshl_b64 s[6:7], s[2:3], 23
	s_waitcnt lgkmcnt(0)
	s_add_u32 s3, s4, s6
	s_addc_u32 s6, s5, s7
	s_lshl_b64 s[4:5], s[92:93], 13
	s_add_u32 s3, s3, s4
	s_addc_u32 s4, s6, s5
	s_lshl_b32 s5, s0, 7
	s_and_b32 s5, s5, 0x1f80
	s_add_u32 s3, s3, s5
	s_addc_u32 s5, s4, 0
	s_add_u32 s4, s3, 0x8000000
	s_addc_u32 s5, s5, 0
	s_mov_b64 s[6:7], 0
